# static wave priority: waves 4-7 (the second wave of each SIMD) raised to priority 1 on entry to the attention phases (indexer, sparse, band); GEMM loops keep their own toggling
# speedup vs baseline: 1.0032x; 1.0032x over previous
.LBB0_356:
	s_or_b64 exec, exec, s[8:9]
	s_waitcnt lgkmcnt(0)
	s_barrier
	s_mov_b32 s4, s78
	v_readfirstlane_b32 s18, v0
	s_bitcmp1_b32 s18, 8
	s_cbranch_scc0 .Lprio_skip
	s_setprio 1
.Lprio_skip:
	s_ashr_i32 s0, s18, 6
	v_writelane_b32 v254, s0, 58
	v_and_b32_e32 v1, 63, v0
	s_nop 0
	v_writelane_b32 v254, s1, 59
	s_nop 0
	v_readlane_b32 s0, v254, 55
	v_readlane_b32 s1, v254, 56
	v_writelane_b32 v254, s4, 60
	s_and_b64 vcc, exec, s[0:1]
	s_mov_b64 s[0:1], -1
	v_writelane_b32 v254, s5, 61
	s_cbranch_vccnz .LBB0_1240
	s_add_u32 s44, s64, 0x10200000
	s_addc_u32 s45, s65, 0
	s_ashr_i32 s63, s62, 31
	s_lshl_b64 s[0:1], s[62:63], 19
	s_add_u32 s0, s64, s0
	s_addc_u32 s1, s65, s1
	s_add_u32 s12, s0, 0x1d200000
	v_writelane_b32 v254, s18, 62
	s_addc_u32 s13, s1, 0
	v_lshlrev_b32_e32 v2, 4, v1
	v_readlane_b32 s0, v254, 15
	s_cmpk_eq_i32 s2, 0x100
	s_cselect_b64 s[48:49], -1, 0
	v_add_u32_e32 v244, s0, v2
	s_sub_i32 s0, 0x1ff, s62
	v_writelane_b32 v254, s0, 63
	s_add_i32 s0, s62, 0x200
	v_writelane_b32 v255, s0, 0
	s_sub_i32 s0, 0x3ff, s62
	v_writelane_b32 v255, s0, 1
	s_movk_i32 s0, 0x4100
	v_readlane_b32 s58, v254, 58
	v_cmp_gt_i32_e64 s[50:51], s0, v0
	s_movk_i32 s0, 0x900
	s_lshl_b32 s66, s58, 5
	v_cmp_gt_i32_e64 s[52:53], s0, v0
	s_mul_i32 s0, s58, 0x1c000
	s_mul_hi_i32 s1, s66, 0xe00
	v_writelane_b32 v255, s0, 2
	s_lshl_b32 s3, s58, 2
	s_or_b32 s54, s3, 1
	v_writelane_b32 v255, s1, 3
	s_lshl_b32 s0, s58, 4
	v_readlane_b32 s1, v254, 16
	s_add_i32 s6, s1, s0
	s_lshl_b32 s0, s54, 2
	s_or_b32 s63, s3, 2
	s_add_i32 s61, s1, s0
	s_lshl_b32 s0, s63, 2
	s_or_b32 s73, s3, 3
	s_add_i32 s71, s1, s0
	s_lshl_b32 s0, s73, 2
	s_add_i32 s79, s1, s0
	s_lshl_b32 s1, s58, 11
	s_add_i32 s80, s58, 8
	s_add_i32 s82, s58, 16
	s_add_i32 s83, s58, 24
	s_add_u32 s16, s64, 0x17200000
	s_addc_u32 s17, s65, 0
	v_add_u32_e32 v242, 0, v2
	v_writelane_b32 v255, s16, 4
	s_lshl_b32 s0, s58, 12
	v_add_u32_e32 v246, s0, v242
	v_writelane_b32 v255, s17, 5
	v_add_u32_e32 v247, s0, v244
	s_add_i32 s0, s66, 0x100
	v_writelane_b32 v255, s0, 6
	v_writelane_b32 v255, s1, 7
	s_add_i32 s0, s1, 0x10000
	v_writelane_b32 v255, s0, 9
	s_add_u32 s0, s64, 0x17200200
	v_writelane_b32 v255, s0, 11
	s_addc_u32 s0, s65, 0
	v_writelane_b32 v255, s0, 12
	s_add_u32 s0, s64, 0x17200400
	v_writelane_b32 v255, s0, 13
	s_addc_u32 s0, s65, 0
	v_writelane_b32 v255, s0, 14
	s_add_u32 s0, s64, 0x17200600
	v_writelane_b32 v255, s0, 15
	s_addc_u32 s0, s65, 0
	v_writelane_b32 v255, s0, 16
	v_readlane_b32 s0, v254, 17
	s_add_i32 s0, s0, s3
	v_readlane_b32 s59, v254, 59
	v_writelane_b32 v255, s0, 17
	s_add_i32 s0, s58, 56
	v_writelane_b32 v255, s0, 18
	s_add_i32 s0, s3, 0
	s_ashr_i32 s59, s58, 31
	v_writelane_b32 v255, s0, 19
	s_lshl_b64 s[0:1], s[58:59], 10
	v_writelane_b32 v255, s0, 20
	v_lshlrev_b32_e32 v241, 2, v1
	v_lshrrev_b32_e32 v243, 4, v1
	v_writelane_b32 v255, s1, 21
	v_writelane_b32 v255, s61, 22
	v_writelane_b32 v255, s63, 23
	v_writelane_b32 v255, s71, 24
	v_writelane_b32 v255, s73, 25
	v_writelane_b32 v255, s79, 26
	s_mov_b32 s0, s58
	v_writelane_b32 v255, s80, 27
	v_writelane_b32 v254, s0, 58
	v_writelane_b32 v255, s82, 28
	v_and_b32_e32 v218, 31, v0
	v_cmp_lt_u32_e64 s[8:9], 15, v1
	s_mov_b32 s60, 0
	v_cmp_eq_u32_e64 s[10:11], 0, v1
	v_cmp_eq_u32_e64 s[20:21], 1, v243
	v_cmp_ne_u32_e64 s[86:87], 1, v243
	v_cmp_eq_u32_e64 s[46:47], 2, v243
	v_or_b32_e32 v245, 3, v241
	s_mul_i32 s4, s58, 0x1040
	s_mul_i32 s57, s54, 0x410
	v_add_u32_e32 v248, 1, v1
	v_writelane_b32 v254, s1, 59
	v_writelane_b32 v255, s83, 29
	s_branch .LBB0_360
